# baseline (speedup 1.0000x reference)
_Z13logits_kernelPKDv8_DF16bS1_PKfS3_PDv2_fS5_Pf:
	s_load_dwordx4 s[4:7], s[0:1], 0x0
	s_load_dwordx4 s[12:15], s[0:1], 0x10
	s_load_dwordx4 s[24:27], s[0:1], 0x20
	s_load_dwordx2 s[28:29], s[0:1], 0x30
	s_lshl_b32 s3, s2, 1
	s_and_b32 s3, s3, 14
	s_ashr_i32 s8, s2, 7
	s_bfe_u32 s10, s2, 0x40003
	s_add_i32 s3, s3, s8
	v_lshrrev_b32_e32 v1, 6, v0
	v_and_b32_e32 v2, 63, v0
	s_movk_i32 s11, 0x3000
	v_add_u32_e32 v6, s10, v1
	v_lshlrev_b32_e32 v2, 4, v2
	v_and_b32_e32 v6, 3, v6
	v_and_b32_e32 v5, 31, v0
	v_mad_u32_u24 v6, v6, s11, v2
	v_lshlrev_b32_e32 v5, 2, v5
	s_mul_i32 s9, s10, 11
	s_lshr_b32 s9, s9, 5
	s_mul_i32 s9, s9, 3
	s_sub_i32 s23, s10, s9
	s_add_i32 s9, s23, 1
	s_cmp_ge_u32 s9, 3
	s_cselect_b32 s30, 0, s9
	s_add_i32 s9, s30, 1
	s_cmp_ge_u32 s9, 3
	s_cselect_b32 s31, 0, s9
	s_lshl_b32 s23, s23, 12
	s_lshl_b32 s30, s30, 12
	s_lshl_b32 s31, s31, 12
	s_lshl_b32 s9, s3, 9
	v_add_u32_e32 v2, s23, v6
	v_add_u32_e32 v3, s30, v6
	v_add_u32_e32 v4, s31, v6
	v_add_u32_e32 v5, s9, v5
	s_mul_i32 s8, s10, 0xc000
	s_mul_i32 s9, s3, 0x30000
	s_waitcnt lgkmcnt(0)
	s_load_dword s22, s[14:15], 0x0
	global_load_dword v248, v5, s[12:13]
	global_load_dword v249, v5, s[12:13] offset:128
	global_load_dword v250, v5, s[12:13] offset:256
	global_load_dword v251, v5, s[12:13] offset:384
	s_add_u32 s4, s4, s8
	s_addc_u32 s5, s5, 0
	s_add_u32 s6, s6, s9
	s_addc_u32 s7, s7, 0
	s_add_u32 s16, s6, 0xc000
	s_addc_u32 s17, s7, 0
	s_add_u32 s18, s6, 0x18000
	s_addc_u32 s19, s7, 0
	s_add_u32 s20, s6, 0x24000
	s_addc_u32 s21, s7, 0
	global_load_dwordx4 v[8:11], v2, s[4:5]
	global_load_dwordx4 v[56:59], v2, s[6:7]
	global_load_dwordx4 v[104:107], v2, s[16:17]
	global_load_dwordx4 v[152:155], v2, s[18:19]
	global_load_dwordx4 v[200:203], v2, s[20:21]
	global_load_dwordx4 v[12:15], v2, s[4:5] offset:1024
	global_load_dwordx4 v[60:63], v2, s[6:7] offset:1024
	global_load_dwordx4 v[108:111], v2, s[16:17] offset:1024
	global_load_dwordx4 v[156:159], v2, s[18:19] offset:1024
	global_load_dwordx4 v[204:207], v2, s[20:21] offset:1024
	global_load_dwordx4 v[16:19], v2, s[4:5] offset:2048
	global_load_dwordx4 v[64:67], v2, s[6:7] offset:2048
	global_load_dwordx4 v[112:115], v2, s[16:17] offset:2048
	global_load_dwordx4 v[160:163], v2, s[18:19] offset:2048
	global_load_dwordx4 v[208:211], v2, s[20:21] offset:2048
	global_load_dwordx4 v[20:23], v2, s[4:5] offset:3072
	global_load_dwordx4 v[68:71], v2, s[6:7] offset:3072
	global_load_dwordx4 v[116:119], v2, s[16:17] offset:3072
	global_load_dwordx4 v[164:167], v2, s[18:19] offset:3072
	global_load_dwordx4 v[212:215], v2, s[20:21] offset:3072
	global_load_dwordx4 v[24:27], v3, s[4:5]
	global_load_dwordx4 v[72:75], v3, s[6:7]
	global_load_dwordx4 v[120:123], v3, s[16:17]
	global_load_dwordx4 v[168:171], v3, s[18:19]
	global_load_dwordx4 v[216:219], v3, s[20:21]
	global_load_dwordx4 v[28:31], v3, s[4:5] offset:1024
	global_load_dwordx4 v[76:79], v3, s[6:7] offset:1024
	global_load_dwordx4 v[124:127], v3, s[16:17] offset:1024
	global_load_dwordx4 v[172:175], v3, s[18:19] offset:1024
	global_load_dwordx4 v[220:223], v3, s[20:21] offset:1024
	global_load_dwordx4 v[32:35], v3, s[4:5] offset:2048
	global_load_dwordx4 v[80:83], v3, s[6:7] offset:2048
	global_load_dwordx4 v[128:131], v3, s[16:17] offset:2048
	global_load_dwordx4 v[176:179], v3, s[18:19] offset:2048
	global_load_dwordx4 v[224:227], v3, s[20:21] offset:2048
	global_load_dwordx4 v[36:39], v3, s[4:5] offset:3072
	global_load_dwordx4 v[84:87], v3, s[6:7] offset:3072
	global_load_dwordx4 v[132:135], v3, s[16:17] offset:3072
	global_load_dwordx4 v[180:183], v3, s[18:19] offset:3072
	global_load_dwordx4 v[228:231], v3, s[20:21] offset:3072
	global_load_dwordx4 v[40:43], v4, s[4:5]
	global_load_dwordx4 v[88:91], v4, s[6:7]
	global_load_dwordx4 v[136:139], v4, s[16:17]
	global_load_dwordx4 v[184:187], v4, s[18:19]
	global_load_dwordx4 v[232:235], v4, s[20:21]
	global_load_dwordx4 v[44:47], v4, s[4:5] offset:1024
	global_load_dwordx4 v[92:95], v4, s[6:7] offset:1024
	global_load_dwordx4 v[140:143], v4, s[16:17] offset:1024
	global_load_dwordx4 v[188:191], v4, s[18:19] offset:1024
	global_load_dwordx4 v[236:239], v4, s[20:21] offset:1024
	global_load_dwordx4 v[48:51], v4, s[4:5] offset:2048
	global_load_dwordx4 v[96:99], v4, s[6:7] offset:2048
	global_load_dwordx4 v[144:147], v4, s[16:17] offset:2048
	global_load_dwordx4 v[192:195], v4, s[18:19] offset:2048
	global_load_dwordx4 v[240:243], v4, s[20:21] offset:2048
	global_load_dwordx4 v[52:55], v4, s[4:5] offset:3072
	global_load_dwordx4 v[100:103], v4, s[6:7] offset:3072
	global_load_dwordx4 v[148:151], v4, s[16:17] offset:3072
	global_load_dwordx4 v[196:199], v4, s[18:19] offset:3072
	global_load_dwordx4 v[244:247], v4, s[20:21] offset:3072
	s_waitcnt vmcnt(58)
	v_mfma_f32_32x32x16_bf16 a[0:15], v[8:11], v[56:59], 0
	s_waitcnt vmcnt(57)
	v_mfma_f32_32x32x16_bf16 a[0:15], v[8:11], v[104:107], a[0:15]
	s_waitcnt vmcnt(56)
	v_mfma_f32_32x32x16_bf16 a[0:15], v[8:11], v[152:155], a[0:15]
	s_waitcnt vmcnt(55)
	v_mfma_f32_32x32x16_bf16 a[0:15], v[8:11], v[200:203], a[0:15]
	s_waitcnt vmcnt(53)
	v_mfma_f32_32x32x16_bf16 a[0:15], v[12:15], v[60:63], a[0:15]
	s_waitcnt vmcnt(52)
	v_mfma_f32_32x32x16_bf16 a[0:15], v[12:15], v[108:111], a[0:15]
	s_waitcnt vmcnt(51)
	v_mfma_f32_32x32x16_bf16 a[0:15], v[12:15], v[156:159], a[0:15]
	s_waitcnt vmcnt(50)
	v_mfma_f32_32x32x16_bf16 a[0:15], v[12:15], v[204:207], a[0:15]
	v_add_f32_e32 v8, 0, v248
	v_add_f32_e32 v8, v8, v249
	v_add_f32_e32 v8, v8, v250
	v_add_f32_e32 v8, v8, v251
	v_mov_b32_e32 v9, 0x3fb8aa3b
	s_waitcnt lgkmcnt(0)
	v_mul_f32_e32 v9, s22, v9
	v_exp_f32_e32 v9, v9
	v_add_f32_e32 v10, 0x2b8cbccc, v8
	v_div_scale_f32 v11, s[8:9], v10, v10, v9
	v_rcp_f32_e32 v12, v11
	v_div_scale_f32 v13, vcc, v9, v10, v9
	v_fma_f32 v14, -v11, v12, 1.0
	v_fmac_f32_e32 v12, v14, v12
	v_mul_f32_e32 v14, v13, v12
	v_fma_f32 v15, -v11, v14, v13
	v_fmac_f32_e32 v14, v15, v12
	v_fma_f32 v11, -v11, v14, v13
	v_div_fmas_f32 v11, v11, v12, v14
	v_div_fixup_f32 v9, v11, v10, v9
	v_lshlrev_b32_e32 v10, 2, v0
	v_add_u32_e32 v10, 0x4000, v10
	v_cmp_gt_u32_e32 vcc, 32, v0
	s_and_saveexec_b64 s[8:9], vcc
	ds_write2_b32 v10, v8, v9 offset0:128 offset1:160
	s_mov_b64 exec, s[8:9]
	s_waitcnt vmcnt(48)
	v_mfma_f32_32x32x16_bf16 a[0:15], v[16:19], v[64:67], a[0:15]
	s_waitcnt vmcnt(47)
	v_mfma_f32_32x32x16_bf16 a[0:15], v[16:19], v[112:115], a[0:15]
	s_waitcnt vmcnt(46)
	v_mfma_f32_32x32x16_bf16 a[0:15], v[16:19], v[160:163], a[0:15]
	s_waitcnt vmcnt(45)
	v_mfma_f32_32x32x16_bf16 a[0:15], v[16:19], v[208:211], a[0:15]
	s_waitcnt vmcnt(43)
	v_mfma_f32_32x32x16_bf16 a[0:15], v[20:23], v[68:71], a[0:15]
	s_waitcnt vmcnt(42)
	v_mfma_f32_32x32x16_bf16 a[0:15], v[20:23], v[116:119], a[0:15]
	s_waitcnt vmcnt(41)
	v_mfma_f32_32x32x16_bf16 a[0:15], v[20:23], v[164:167], a[0:15]
	s_waitcnt vmcnt(40)
	v_mfma_f32_32x32x16_bf16 a[0:15], v[20:23], v[212:215], a[0:15]
	s_waitcnt vmcnt(38)
	v_mfma_f32_32x32x16_bf16 a[0:15], v[24:27], v[72:75], a[0:15]
	s_waitcnt vmcnt(37)
	v_mfma_f32_32x32x16_bf16 a[0:15], v[24:27], v[120:123], a[0:15]
	s_waitcnt vmcnt(36)
	v_mfma_f32_32x32x16_bf16 a[0:15], v[24:27], v[168:171], a[0:15]
	s_waitcnt vmcnt(35)
	v_mfma_f32_32x32x16_bf16 a[0:15], v[24:27], v[216:219], a[0:15]
	s_waitcnt vmcnt(33)
	v_mfma_f32_32x32x16_bf16 a[0:15], v[28:31], v[76:79], a[0:15]
	s_waitcnt vmcnt(32)
	v_mfma_f32_32x32x16_bf16 a[0:15], v[28:31], v[124:127], a[0:15]
	s_waitcnt vmcnt(31)
	v_mfma_f32_32x32x16_bf16 a[0:15], v[28:31], v[172:175], a[0:15]
	s_waitcnt vmcnt(30)
	v_mfma_f32_32x32x16_bf16 a[0:15], v[28:31], v[220:223], a[0:15]
	s_waitcnt vmcnt(28)
	v_mfma_f32_32x32x16_bf16 a[0:15], v[32:35], v[80:83], a[0:15]
	s_waitcnt vmcnt(27)
	v_mfma_f32_32x32x16_bf16 a[0:15], v[32:35], v[128:131], a[0:15]
	s_waitcnt vmcnt(26)
	v_mfma_f32_32x32x16_bf16 a[0:15], v[32:35], v[176:179], a[0:15]
	s_waitcnt vmcnt(25)
	v_mfma_f32_32x32x16_bf16 a[0:15], v[32:35], v[224:227], a[0:15]
	s_waitcnt vmcnt(23)
	v_mfma_f32_32x32x16_bf16 a[0:15], v[36:39], v[84:87], a[0:15]
	s_waitcnt vmcnt(22)
	v_mfma_f32_32x32x16_bf16 a[0:15], v[36:39], v[132:135], a[0:15]
	s_waitcnt vmcnt(21)
	v_mfma_f32_32x32x16_bf16 a[0:15], v[36:39], v[180:183], a[0:15]
	s_waitcnt vmcnt(20)
	v_mfma_f32_32x32x16_bf16 a[0:15], v[36:39], v[228:231], a[0:15]
	s_waitcnt vmcnt(18)
	v_mfma_f32_32x32x16_bf16 a[0:15], v[40:43], v[88:91], a[0:15]
	s_waitcnt vmcnt(17)
	v_mfma_f32_32x32x16_bf16 a[0:15], v[40:43], v[136:139], a[0:15]
	s_waitcnt vmcnt(16)
	v_mfma_f32_32x32x16_bf16 a[0:15], v[40:43], v[184:187], a[0:15]
	s_waitcnt vmcnt(15)
	v_mfma_f32_32x32x16_bf16 a[0:15], v[40:43], v[232:235], a[0:15]
	s_waitcnt vmcnt(13)
	v_mfma_f32_32x32x16_bf16 a[0:15], v[44:47], v[92:95], a[0:15]
	s_waitcnt vmcnt(12)
	v_mfma_f32_32x32x16_bf16 a[0:15], v[44:47], v[140:143], a[0:15]
	s_waitcnt vmcnt(11)
	v_mfma_f32_32x32x16_bf16 a[0:15], v[44:47], v[188:191], a[0:15]
	s_waitcnt vmcnt(10)
	v_mfma_f32_32x32x16_bf16 a[0:15], v[44:47], v[236:239], a[0:15]
	s_waitcnt vmcnt(8)
	v_mfma_f32_32x32x16_bf16 a[0:15], v[48:51], v[96:99], a[0:15]
	s_waitcnt vmcnt(7)
	v_mfma_f32_32x32x16_bf16 a[0:15], v[48:51], v[144:147], a[0:15]
	s_waitcnt vmcnt(6)
	v_mfma_f32_32x32x16_bf16 a[0:15], v[48:51], v[192:195], a[0:15]
	s_waitcnt vmcnt(5)
	v_mfma_f32_32x32x16_bf16 a[0:15], v[48:51], v[240:243], a[0:15]
	v_mul_u32_u24_e32 v1, 0x1080, v1
	s_movk_i32 s4, 0x7f
	s_movk_i32 s6, 0x84
	v_cmp_lt_u32_e32 vcc, s4, v0
	v_lshrrev_b32_e32 v11, 3, v0
	v_and_b32_e32 v10, 31, v0
	v_and_b32_e32 v11, 4, v11
	v_mul_u32_u24_e32 v11, 0x84, v11
	v_lshlrev_b32_e32 v9, 2, v10
	v_bfe_u32 v6, v0, 2, 5
	v_and_b32_e32 v7, 3, v0
	v_add3_u32 v1, v1, v11, v9
	v_lshlrev_b32_e32 v8, 3, v7
	s_waitcnt vmcnt(3)
	v_mfma_f32_32x32x16_bf16 a[0:15], v[52:55], v[100:103], a[0:15]
	s_waitcnt vmcnt(2)
	v_mfma_f32_32x32x16_bf16 a[0:15], v[52:55], v[148:151], a[0:15]
	s_waitcnt vmcnt(1)
	v_mfma_f32_32x32x16_bf16 a[0:15], v[52:55], v[196:199], a[0:15]
	s_waitcnt vmcnt(0)
	v_mfma_f32_32x32x16_bf16 a[0:15], v[52:55], v[244:247], a[0:15]
	s_nop 11
	ds_write_b32 v1, a0
	ds_write_b32 v1, a1 offset:132
	ds_write_b32 v1, a2 offset:264
	ds_write_b32 v1, a3 offset:396
	ds_write_b32 v1, a4 offset:1056
	ds_write_b32 v1, a5 offset:1188
	ds_write_b32 v1, a6 offset:1320
	ds_write_b32 v1, a7 offset:1452
	ds_write_b32 v1, a8 offset:2112
	ds_write_b32 v1, a9 offset:2244
	ds_write_b32 v1, a10 offset:2376
	ds_write_b32 v1, a11 offset:2508
	ds_write_b32 v1, a12 offset:3168
	ds_write_b32 v1, a13 offset:3300
	ds_write_b32 v1, a14 offset:3432
	ds_write_b32 v1, a15 offset:3564
	v_bfe_u32 v6, v0, 2, 5
	v_and_b32_e32 v7, 3, v0
	v_lshlrev_b32_e32 v9, 3, v7
	v_readfirstlane_b32 s30, v0
	v_sub_u32_e32 v10, v6, v9
	s_waitcnt lgkmcnt(0)
	s_barrier
	s_cmpk_ge_u32 s30, 0x80
	s_cbranch_scc1 .Llg_k1
	v_mul_u32_u24_e32 v2, 0x84, v6
	v_lshlrev_b32_e32 v8, 5, v7
	v_add_u32_e32 v2, v2, v8
	v_add_u32_e32 v8, 0x4280, v8
	v_add_u32_e32 v3, 0x1080, v2
	v_add_u32_e32 v4, 0x2100, v2
	v_add_u32_e32 v5, 0x3180, v2
	ds_read_b128 v[48:51], v8
	ds_read_b128 v[52:55], v8 offset:16
	ds_read2_b32 v[16:17], v2 offset0:0 offset1:1
	ds_read2_b32 v[18:19], v2 offset0:2 offset1:3
	ds_read2_b32 v[20:21], v2 offset0:4 offset1:5
	ds_read2_b32 v[22:23], v2 offset0:6 offset1:7
	ds_read2_b32 v[24:25], v3 offset0:0 offset1:1
	ds_read2_b32 v[26:27], v3 offset0:2 offset1:3
	ds_read2_b32 v[28:29], v3 offset0:4 offset1:5
	ds_read2_b32 v[30:31], v3 offset0:6 offset1:7
	ds_read2_b32 v[32:33], v4 offset0:0 offset1:1
	ds_read2_b32 v[34:35], v4 offset0:2 offset1:3
	ds_read2_b32 v[36:37], v4 offset0:4 offset1:5
	ds_read2_b32 v[38:39], v4 offset0:6 offset1:7
	s_waitcnt lgkmcnt(4)
	ds_read2_b32 v[40:41], v5 offset0:0 offset1:1
	ds_read2_b32 v[42:43], v5 offset0:2 offset1:3
	ds_read2_b32 v[44:45], v5 offset0:4 offset1:5
	ds_read2_b32 v[46:47], v5 offset0:6 offset1:7
	s_waitcnt lgkmcnt(0)
	s_branch .Llg_join

	.amdhsa_kernel _Z13logits_kernelPKDv8_DF16bS1_PKfS3_PDv2_fS5_Pf
		.amdhsa_group_segment_fixed_size 17152
		.amdhsa_private_segment_fixed_size 0
		.amdhsa_kernarg_size 56
		.amdhsa_user_sgpr_count 2
		.amdhsa_user_sgpr_dispatch_ptr 0
		.amdhsa_user_sgpr_queue_ptr 0
		.amdhsa_user_sgpr_kernarg_segment_ptr 1
		.amdhsa_user_sgpr_dispatch_id 0
		.amdhsa_user_sgpr_kernarg_preload_length 0
		.amdhsa_user_sgpr_kernarg_preload_offset 0
		.amdhsa_user_sgpr_private_segment_size 0
		.amdhsa_uses_dynamic_stack 0
		.amdhsa_enable_private_segment 0
		.amdhsa_system_sgpr_workgroup_id_x 1
		.amdhsa_system_sgpr_workgroup_id_y 0
		.amdhsa_system_sgpr_workgroup_id_z 0
		.amdhsa_system_sgpr_workgroup_info 0
		.amdhsa_system_vgpr_workitem_id 0
		.amdhsa_next_free_vgpr 268
		.amdhsa_next_free_sgpr 32
		.amdhsa_accum_offset 252
		.amdhsa_reserve_vcc 1
		.amdhsa_float_round_mode_32 0
		.amdhsa_float_round_mode_16_64 0
		.amdhsa_float_denorm_mode_32 3
		.amdhsa_float_denorm_mode_16_64 3
		.amdhsa_dx10_clamp 1
		.amdhsa_ieee_mode 1
		.amdhsa_fp16_overflow 0
		.amdhsa_tg_split 0
		.amdhsa_exception_fp_ieee_invalid_op 0
		.amdhsa_exception_fp_denorm_src 0
		.amdhsa_exception_fp_ieee_div_zero 0
		.amdhsa_exception_fp_ieee_overflow 0
		.amdhsa_exception_fp_ieee_underflow 0
		.amdhsa_exception_fp_ieee_inexact 0
		.amdhsa_exception_int_div_zero 0
	.end_amdhsa_kernel
